# speedup vs baseline: 1.0029x; 1.0029x over previous
_Z9k_combinePKDF16_PK15HIP_vector_typeIiLj2EEPKS1_IfLj2EEPf:
	s_load_dwordx4 s[4:7], s[0:1], 0x0
	s_load_dwordx4 s[8:11], s[0:1], 0x10
	v_readfirstlane_b32 s12, v0
	v_and_b32_e32 v1, 0x7f, v0
	s_lshl_b32 s13, s2, 1
	v_lshlrev_b32_e32 v2, 4, v1
	v_lshlrev_b32_e32 v3, 5, v1
	s_lshr_b32 s12, s12, 7
	s_or_b32 s12, s13, s12
	s_lshl_b32 s13, s12, 3
	s_lshl_b32 s22, s12, 12
	s_waitcnt lgkmcnt(0)
	s_load_dwordx2 s[14:15], s[6:7], s13
	s_load_dwordx2 s[16:17], s[8:9], s13
	v_lshrrev_b32_e32 v4, 5, v1
	v_and_b32_e32 v5, 31, v1
	v_lshlrev_b32_e32 v4, 20, v4
	v_lshl_or_b32 v4, v5, 4, v4
	s_add_u32 s10, s10, s22
	s_addc_u32 s11, s11, 0
	s_waitcnt lgkmcnt(0)
	s_lshr_b32 s18, s14, 8
	s_lshr_b32 s19, s15, 8
	s_cmp_gt_u32 s18, 63
	s_cbranch_scc1 .Lcmb_a
	s_lshl_b32 s20, s14, 11
	s_add_u32 s20, s4, s20
	s_addc_u32 s21, s5, 0
	global_load_dwordx4 v[8:11], v2, s[20:21]
.Lcmb_a:
	s_cmp_gt_u32 s19, 63
	s_cbranch_scc1 .Lcmb_b
	s_lshl_b32 s20, s15, 11
	s_add_u32 s20, s4, s20
	s_addc_u32 s21, s5, 0
	global_load_dwordx4 v[12:15], v2, s[20:21]
.Lcmb_b:
	s_cmp_gt_u32 s18, 63
	s_cbranch_scc1 .Lcmb_slab0
	s_waitcnt vmcnt(0)
	v_cvt_f32_f16_e32 v48, v8
	v_cvt_f32_f16_sdwa v49, v8 dst_sel:DWORD dst_unused:UNUSED_PAD src0_sel:WORD_1
	v_cvt_f32_f16_e32 v50, v9
	v_cvt_f32_f16_sdwa v51, v9 dst_sel:DWORD dst_unused:UNUSED_PAD src0_sel:WORD_1
	v_cvt_f32_f16_e32 v52, v10
	v_cvt_f32_f16_sdwa v53, v10 dst_sel:DWORD dst_unused:UNUSED_PAD src0_sel:WORD_1
	v_cvt_f32_f16_e32 v54, v11
	v_cvt_f32_f16_sdwa v55, v11 dst_sel:DWORD dst_unused:UNUSED_PAD src0_sel:WORD_1
	s_branch .Lcmb_m0
.Lcmb_slab0:
	s_sub_u32 s20, s18, 64
	s_lshl_b32 s20, s20, 22
	s_and_b32 s22, s14, 0xff
	s_lshl_b32 s22, s22, 9
	s_add_u32 s20, s20, s22
	s_add_u32 s20, s20, 0x2400000
	s_add_u32 s20, s4, s20
	s_addc_u32 s21, s5, 0
	global_load_dwordx4 v[16:19], v4, s[20:21]
	s_add_u32 s20, s20, 0x20000
	s_addc_u32 s21, s21, 0
	global_load_dwordx4 v[20:23], v4, s[20:21]
	s_add_u32 s20, s20, 0x20000
	s_addc_u32 s21, s21, 0
	global_load_dwordx4 v[24:27], v4, s[20:21]
	s_add_u32 s20, s20, 0x20000
	s_addc_u32 s21, s21, 0
	global_load_dwordx4 v[28:31], v4, s[20:21]
	s_add_u32 s20, s20, 0x20000
	s_addc_u32 s21, s21, 0
	global_load_dwordx4 v[32:35], v4, s[20:21]
	s_add_u32 s20, s20, 0x20000
	s_addc_u32 s21, s21, 0
	global_load_dwordx4 v[36:39], v4, s[20:21]
	s_add_u32 s20, s20, 0x20000
	s_addc_u32 s21, s21, 0
	global_load_dwordx4 v[40:43], v4, s[20:21]
	s_add_u32 s20, s20, 0x20000
	s_addc_u32 s21, s21, 0
	global_load_dwordx4 v[44:47], v4, s[20:21]
	s_waitcnt vmcnt(0)
	v_cvt_f32_f16_e32 v48, v16
	v_cvt_f32_f16_sdwa v49, v16 dst_sel:DWORD dst_unused:UNUSED_PAD src0_sel:WORD_1
	v_cvt_f32_f16_e32 v50, v17
	v_cvt_f32_f16_sdwa v51, v17 dst_sel:DWORD dst_unused:UNUSED_PAD src0_sel:WORD_1
	v_cvt_f32_f16_e32 v52, v18
	v_cvt_f32_f16_sdwa v53, v18 dst_sel:DWORD dst_unused:UNUSED_PAD src0_sel:WORD_1
	v_cvt_f32_f16_e32 v54, v19
	v_cvt_f32_f16_sdwa v55, v19 dst_sel:DWORD dst_unused:UNUSED_PAD src0_sel:WORD_1
	v_cvt_f32_f16_e32 v5, v20
	v_cvt_f32_f16_sdwa v6, v20 dst_sel:DWORD dst_unused:UNUSED_PAD src0_sel:WORD_1
	v_add_f32_e32 v48, v48, v5
	v_add_f32_e32 v49, v49, v6
	v_cvt_f32_f16_e32 v5, v21
	v_cvt_f32_f16_sdwa v6, v21 dst_sel:DWORD dst_unused:UNUSED_PAD src0_sel:WORD_1
	v_add_f32_e32 v50, v50, v5
	v_add_f32_e32 v51, v51, v6
	v_cvt_f32_f16_e32 v5, v22
	v_cvt_f32_f16_sdwa v6, v22 dst_sel:DWORD dst_unused:UNUSED_PAD src0_sel:WORD_1
	v_add_f32_e32 v52, v52, v5
	v_add_f32_e32 v53, v53, v6
	v_cvt_f32_f16_e32 v5, v23
	v_cvt_f32_f16_sdwa v6, v23 dst_sel:DWORD dst_unused:UNUSED_PAD src0_sel:WORD_1
	v_add_f32_e32 v54, v54, v5
	v_add_f32_e32 v55, v55, v6
	v_cvt_f32_f16_e32 v5, v24
	v_cvt_f32_f16_sdwa v6, v24 dst_sel:DWORD dst_unused:UNUSED_PAD src0_sel:WORD_1
	v_add_f32_e32 v48, v48, v5
	v_add_f32_e32 v49, v49, v6
	v_cvt_f32_f16_e32 v5, v25
	v_cvt_f32_f16_sdwa v6, v25 dst_sel:DWORD dst_unused:UNUSED_PAD src0_sel:WORD_1
	v_add_f32_e32 v50, v50, v5
	v_add_f32_e32 v51, v51, v6
	v_cvt_f32_f16_e32 v5, v26
	v_cvt_f32_f16_sdwa v6, v26 dst_sel:DWORD dst_unused:UNUSED_PAD src0_sel:WORD_1
	v_add_f32_e32 v52, v52, v5
	v_add_f32_e32 v53, v53, v6
	v_cvt_f32_f16_e32 v5, v27
	v_cvt_f32_f16_sdwa v6, v27 dst_sel:DWORD dst_unused:UNUSED_PAD src0_sel:WORD_1
	v_add_f32_e32 v54, v54, v5
	v_add_f32_e32 v55, v55, v6
	v_cvt_f32_f16_e32 v5, v28
	v_cvt_f32_f16_sdwa v6, v28 dst_sel:DWORD dst_unused:UNUSED_PAD src0_sel:WORD_1
	v_add_f32_e32 v48, v48, v5
	v_add_f32_e32 v49, v49, v6
	v_cvt_f32_f16_e32 v5, v29
	v_cvt_f32_f16_sdwa v6, v29 dst_sel:DWORD dst_unused:UNUSED_PAD src0_sel:WORD_1
	v_add_f32_e32 v50, v50, v5
	v_add_f32_e32 v51, v51, v6
	v_cvt_f32_f16_e32 v5, v30
	v_cvt_f32_f16_sdwa v6, v30 dst_sel:DWORD dst_unused:UNUSED_PAD src0_sel:WORD_1
	v_add_f32_e32 v52, v52, v5
	v_add_f32_e32 v53, v53, v6
	v_cvt_f32_f16_e32 v5, v31
	v_cvt_f32_f16_sdwa v6, v31 dst_sel:DWORD dst_unused:UNUSED_PAD src0_sel:WORD_1
	v_add_f32_e32 v54, v54, v5
	v_add_f32_e32 v55, v55, v6
	v_cvt_f32_f16_e32 v5, v32
	v_cvt_f32_f16_sdwa v6, v32 dst_sel:DWORD dst_unused:UNUSED_PAD src0_sel:WORD_1
	v_add_f32_e32 v48, v48, v5
	v_add_f32_e32 v49, v49, v6
	v_cvt_f32_f16_e32 v5, v33
	v_cvt_f32_f16_sdwa v6, v33 dst_sel:DWORD dst_unused:UNUSED_PAD src0_sel:WORD_1
	v_add_f32_e32 v50, v50, v5
	v_add_f32_e32 v51, v51, v6
	v_cvt_f32_f16_e32 v5, v34
	v_cvt_f32_f16_sdwa v6, v34 dst_sel:DWORD dst_unused:UNUSED_PAD src0_sel:WORD_1
	v_add_f32_e32 v52, v52, v5
	v_add_f32_e32 v53, v53, v6
	v_cvt_f32_f16_e32 v5, v35
	v_cvt_f32_f16_sdwa v6, v35 dst_sel:DWORD dst_unused:UNUSED_PAD src0_sel:WORD_1
	v_add_f32_e32 v54, v54, v5
	v_add_f32_e32 v55, v55, v6
	v_cvt_f32_f16_e32 v5, v36
	v_cvt_f32_f16_sdwa v6, v36 dst_sel:DWORD dst_unused:UNUSED_PAD src0_sel:WORD_1
	v_add_f32_e32 v48, v48, v5
	v_add_f32_e32 v49, v49, v6
	v_cvt_f32_f16_e32 v5, v37
	v_cvt_f32_f16_sdwa v6, v37 dst_sel:DWORD dst_unused:UNUSED_PAD src0_sel:WORD_1
	v_add_f32_e32 v50, v50, v5
	v_add_f32_e32 v51, v51, v6
	v_cvt_f32_f16_e32 v5, v38
	v_cvt_f32_f16_sdwa v6, v38 dst_sel:DWORD dst_unused:UNUSED_PAD src0_sel:WORD_1
	v_add_f32_e32 v52, v52, v5
	v_add_f32_e32 v53, v53, v6
	v_cvt_f32_f16_e32 v5, v39
	v_cvt_f32_f16_sdwa v6, v39 dst_sel:DWORD dst_unused:UNUSED_PAD src0_sel:WORD_1
	v_add_f32_e32 v54, v54, v5
	v_add_f32_e32 v55, v55, v6
	v_cvt_f32_f16_e32 v5, v40
	v_cvt_f32_f16_sdwa v6, v40 dst_sel:DWORD dst_unused:UNUSED_PAD src0_sel:WORD_1
	v_add_f32_e32 v48, v48, v5
	v_add_f32_e32 v49, v49, v6
	v_cvt_f32_f16_e32 v5, v41
	v_cvt_f32_f16_sdwa v6, v41 dst_sel:DWORD dst_unused:UNUSED_PAD src0_sel:WORD_1
	v_add_f32_e32 v50, v50, v5
	v_add_f32_e32 v51, v51, v6
	v_cvt_f32_f16_e32 v5, v42
	v_cvt_f32_f16_sdwa v6, v42 dst_sel:DWORD dst_unused:UNUSED_PAD src0_sel:WORD_1
	v_add_f32_e32 v52, v52, v5
	v_add_f32_e32 v53, v53, v6
	v_cvt_f32_f16_e32 v5, v43
	v_cvt_f32_f16_sdwa v6, v43 dst_sel:DWORD dst_unused:UNUSED_PAD src0_sel:WORD_1
	v_add_f32_e32 v54, v54, v5
	v_add_f32_e32 v55, v55, v6
	v_cvt_f32_f16_e32 v5, v44
	v_cvt_f32_f16_sdwa v6, v44 dst_sel:DWORD dst_unused:UNUSED_PAD src0_sel:WORD_1
	v_add_f32_e32 v48, v48, v5
	v_add_f32_e32 v49, v49, v6
	v_cvt_f32_f16_e32 v5, v45
	v_cvt_f32_f16_sdwa v6, v45 dst_sel:DWORD dst_unused:UNUSED_PAD src0_sel:WORD_1
	v_add_f32_e32 v50, v50, v5
	v_add_f32_e32 v51, v51, v6
	v_cvt_f32_f16_e32 v5, v46
	v_cvt_f32_f16_sdwa v6, v46 dst_sel:DWORD dst_unused:UNUSED_PAD src0_sel:WORD_1
	v_add_f32_e32 v52, v52, v5
	v_add_f32_e32 v53, v53, v6
	v_cvt_f32_f16_e32 v5, v47
	v_cvt_f32_f16_sdwa v6, v47 dst_sel:DWORD dst_unused:UNUSED_PAD src0_sel:WORD_1
	v_add_f32_e32 v54, v54, v5
	v_add_f32_e32 v55, v55, v6
.Lcmb_m0:
	v_mul_f32_e32 v56, s16, v48
	v_mul_f32_e32 v57, s16, v49
	v_mul_f32_e32 v58, s16, v50
	v_mul_f32_e32 v59, s16, v51
	v_mul_f32_e32 v60, s16, v52
	v_mul_f32_e32 v61, s16, v53
	v_mul_f32_e32 v62, s16, v54
	v_mul_f32_e32 v63, s16, v55
	s_cmp_gt_u32 s19, 63
	s_cbranch_scc1 .Lcmb_slab1
	v_cvt_f32_f16_e32 v48, v12
	v_cvt_f32_f16_sdwa v49, v12 dst_sel:DWORD dst_unused:UNUSED_PAD src0_sel:WORD_1
	v_cvt_f32_f16_e32 v50, v13
	v_cvt_f32_f16_sdwa v51, v13 dst_sel:DWORD dst_unused:UNUSED_PAD src0_sel:WORD_1
	v_cvt_f32_f16_e32 v52, v14
	v_cvt_f32_f16_sdwa v53, v14 dst_sel:DWORD dst_unused:UNUSED_PAD src0_sel:WORD_1
	v_cvt_f32_f16_e32 v54, v15
	v_cvt_f32_f16_sdwa v55, v15 dst_sel:DWORD dst_unused:UNUSED_PAD src0_sel:WORD_1
	s_branch .Lcmb_m1
.Lcmb_slab1:
	s_sub_u32 s20, s19, 64
	s_lshl_b32 s20, s20, 22
	s_and_b32 s22, s15, 0xff
	s_lshl_b32 s22, s22, 9
	s_add_u32 s20, s20, s22
	s_add_u32 s20, s20, 0x2400000
	s_add_u32 s20, s4, s20
	s_addc_u32 s21, s5, 0
	global_load_dwordx4 v[16:19], v4, s[20:21]
	s_add_u32 s20, s20, 0x20000
	s_addc_u32 s21, s21, 0
	global_load_dwordx4 v[20:23], v4, s[20:21]
	s_add_u32 s20, s20, 0x20000
	s_addc_u32 s21, s21, 0
	global_load_dwordx4 v[24:27], v4, s[20:21]
	s_add_u32 s20, s20, 0x20000
	s_addc_u32 s21, s21, 0
	global_load_dwordx4 v[28:31], v4, s[20:21]
	s_add_u32 s20, s20, 0x20000
	s_addc_u32 s21, s21, 0
	global_load_dwordx4 v[32:35], v4, s[20:21]
	s_add_u32 s20, s20, 0x20000
	s_addc_u32 s21, s21, 0
	global_load_dwordx4 v[36:39], v4, s[20:21]
	s_add_u32 s20, s20, 0x20000
	s_addc_u32 s21, s21, 0
	global_load_dwordx4 v[40:43], v4, s[20:21]
	s_add_u32 s20, s20, 0x20000
	s_addc_u32 s21, s21, 0
	global_load_dwordx4 v[44:47], v4, s[20:21]
	s_waitcnt vmcnt(0)
	v_cvt_f32_f16_e32 v48, v16
	v_cvt_f32_f16_sdwa v49, v16 dst_sel:DWORD dst_unused:UNUSED_PAD src0_sel:WORD_1
	v_cvt_f32_f16_e32 v50, v17
	v_cvt_f32_f16_sdwa v51, v17 dst_sel:DWORD dst_unused:UNUSED_PAD src0_sel:WORD_1
	v_cvt_f32_f16_e32 v52, v18
	v_cvt_f32_f16_sdwa v53, v18 dst_sel:DWORD dst_unused:UNUSED_PAD src0_sel:WORD_1
	v_cvt_f32_f16_e32 v54, v19
	v_cvt_f32_f16_sdwa v55, v19 dst_sel:DWORD dst_unused:UNUSED_PAD src0_sel:WORD_1
	v_cvt_f32_f16_e32 v5, v20
	v_cvt_f32_f16_sdwa v6, v20 dst_sel:DWORD dst_unused:UNUSED_PAD src0_sel:WORD_1
	v_add_f32_e32 v48, v48, v5
	v_add_f32_e32 v49, v49, v6
	v_cvt_f32_f16_e32 v5, v21
	v_cvt_f32_f16_sdwa v6, v21 dst_sel:DWORD dst_unused:UNUSED_PAD src0_sel:WORD_1
	v_add_f32_e32 v50, v50, v5
	v_add_f32_e32 v51, v51, v6
	v_cvt_f32_f16_e32 v5, v22
	v_cvt_f32_f16_sdwa v6, v22 dst_sel:DWORD dst_unused:UNUSED_PAD src0_sel:WORD_1
	v_add_f32_e32 v52, v52, v5
	v_add_f32_e32 v53, v53, v6
	v_cvt_f32_f16_e32 v5, v23
	v_cvt_f32_f16_sdwa v6, v23 dst_sel:DWORD dst_unused:UNUSED_PAD src0_sel:WORD_1
	v_add_f32_e32 v54, v54, v5
	v_add_f32_e32 v55, v55, v6
	v_cvt_f32_f16_e32 v5, v24
	v_cvt_f32_f16_sdwa v6, v24 dst_sel:DWORD dst_unused:UNUSED_PAD src0_sel:WORD_1
	v_add_f32_e32 v48, v48, v5
	v_add_f32_e32 v49, v49, v6
	v_cvt_f32_f16_e32 v5, v25
	v_cvt_f32_f16_sdwa v6, v25 dst_sel:DWORD dst_unused:UNUSED_PAD src0_sel:WORD_1
	v_add_f32_e32 v50, v50, v5
	v_add_f32_e32 v51, v51, v6
	v_cvt_f32_f16_e32 v5, v26
	v_cvt_f32_f16_sdwa v6, v26 dst_sel:DWORD dst_unused:UNUSED_PAD src0_sel:WORD_1
	v_add_f32_e32 v52, v52, v5
	v_add_f32_e32 v53, v53, v6
	v_cvt_f32_f16_e32 v5, v27
	v_cvt_f32_f16_sdwa v6, v27 dst_sel:DWORD dst_unused:UNUSED_PAD src0_sel:WORD_1
	v_add_f32_e32 v54, v54, v5
	v_add_f32_e32 v55, v55, v6
	v_cvt_f32_f16_e32 v5, v28
	v_cvt_f32_f16_sdwa v6, v28 dst_sel:DWORD dst_unused:UNUSED_PAD src0_sel:WORD_1
	v_add_f32_e32 v48, v48, v5
	v_add_f32_e32 v49, v49, v6
	v_cvt_f32_f16_e32 v5, v29
	v_cvt_f32_f16_sdwa v6, v29 dst_sel:DWORD dst_unused:UNUSED_PAD src0_sel:WORD_1
	v_add_f32_e32 v50, v50, v5
	v_add_f32_e32 v51, v51, v6
	v_cvt_f32_f16_e32 v5, v30
	v_cvt_f32_f16_sdwa v6, v30 dst_sel:DWORD dst_unused:UNUSED_PAD src0_sel:WORD_1
	v_add_f32_e32 v52, v52, v5
	v_add_f32_e32 v53, v53, v6
	v_cvt_f32_f16_e32 v5, v31
	v_cvt_f32_f16_sdwa v6, v31 dst_sel:DWORD dst_unused:UNUSED_PAD src0_sel:WORD_1
	v_add_f32_e32 v54, v54, v5
	v_add_f32_e32 v55, v55, v6
	v_cvt_f32_f16_e32 v5, v32
	v_cvt_f32_f16_sdwa v6, v32 dst_sel:DWORD dst_unused:UNUSED_PAD src0_sel:WORD_1
	v_add_f32_e32 v48, v48, v5
	v_add_f32_e32 v49, v49, v6
	v_cvt_f32_f16_e32 v5, v33
	v_cvt_f32_f16_sdwa v6, v33 dst_sel:DWORD dst_unused:UNUSED_PAD src0_sel:WORD_1
	v_add_f32_e32 v50, v50, v5
	v_add_f32_e32 v51, v51, v6
	v_cvt_f32_f16_e32 v5, v34
	v_cvt_f32_f16_sdwa v6, v34 dst_sel:DWORD dst_unused:UNUSED_PAD src0_sel:WORD_1
	v_add_f32_e32 v52, v52, v5
	v_add_f32_e32 v53, v53, v6
	v_cvt_f32_f16_e32 v5, v35
	v_cvt_f32_f16_sdwa v6, v35 dst_sel:DWORD dst_unused:UNUSED_PAD src0_sel:WORD_1
	v_add_f32_e32 v54, v54, v5
	v_add_f32_e32 v55, v55, v6
	v_cvt_f32_f16_e32 v5, v36
	v_cvt_f32_f16_sdwa v6, v36 dst_sel:DWORD dst_unused:UNUSED_PAD src0_sel:WORD_1
	v_add_f32_e32 v48, v48, v5
	v_add_f32_e32 v49, v49, v6
	v_cvt_f32_f16_e32 v5, v37
	v_cvt_f32_f16_sdwa v6, v37 dst_sel:DWORD dst_unused:UNUSED_PAD src0_sel:WORD_1
	v_add_f32_e32 v50, v50, v5
	v_add_f32_e32 v51, v51, v6
	v_cvt_f32_f16_e32 v5, v38
	v_cvt_f32_f16_sdwa v6, v38 dst_sel:DWORD dst_unused:UNUSED_PAD src0_sel:WORD_1
	v_add_f32_e32 v52, v52, v5
	v_add_f32_e32 v53, v53, v6
	v_cvt_f32_f16_e32 v5, v39
	v_cvt_f32_f16_sdwa v6, v39 dst_sel:DWORD dst_unused:UNUSED_PAD src0_sel:WORD_1
	v_add_f32_e32 v54, v54, v5
	v_add_f32_e32 v55, v55, v6
	v_cvt_f32_f16_e32 v5, v40
	v_cvt_f32_f16_sdwa v6, v40 dst_sel:DWORD dst_unused:UNUSED_PAD src0_sel:WORD_1
	v_add_f32_e32 v48, v48, v5
	v_add_f32_e32 v49, v49, v6
	v_cvt_f32_f16_e32 v5, v41
	v_cvt_f32_f16_sdwa v6, v41 dst_sel:DWORD dst_unused:UNUSED_PAD src0_sel:WORD_1
	v_add_f32_e32 v50, v50, v5
	v_add_f32_e32 v51, v51, v6
	v_cvt_f32_f16_e32 v5, v42
	v_cvt_f32_f16_sdwa v6, v42 dst_sel:DWORD dst_unused:UNUSED_PAD src0_sel:WORD_1
	v_add_f32_e32 v52, v52, v5
	v_add_f32_e32 v53, v53, v6
	v_cvt_f32_f16_e32 v5, v43
	v_cvt_f32_f16_sdwa v6, v43 dst_sel:DWORD dst_unused:UNUSED_PAD src0_sel:WORD_1
	v_add_f32_e32 v54, v54, v5
	v_add_f32_e32 v55, v55, v6
	v_cvt_f32_f16_e32 v5, v44
	v_cvt_f32_f16_sdwa v6, v44 dst_sel:DWORD dst_unused:UNUSED_PAD src0_sel:WORD_1
	v_add_f32_e32 v48, v48, v5
	v_add_f32_e32 v49, v49, v6
	v_cvt_f32_f16_e32 v5, v45
	v_cvt_f32_f16_sdwa v6, v45 dst_sel:DWORD dst_unused:UNUSED_PAD src0_sel:WORD_1
	v_add_f32_e32 v50, v50, v5
	v_add_f32_e32 v51, v51, v6
	v_cvt_f32_f16_e32 v5, v46
	v_cvt_f32_f16_sdwa v6, v46 dst_sel:DWORD dst_unused:UNUSED_PAD src0_sel:WORD_1
	v_add_f32_e32 v52, v52, v5
	v_add_f32_e32 v53, v53, v6
	v_cvt_f32_f16_e32 v5, v47
	v_cvt_f32_f16_sdwa v6, v47 dst_sel:DWORD dst_unused:UNUSED_PAD src0_sel:WORD_1
	v_add_f32_e32 v54, v54, v5
	v_add_f32_e32 v55, v55, v6
.Lcmb_m1:
	v_fmac_f32_e32 v56, s17, v48
	v_fmac_f32_e32 v57, s17, v49
	v_fmac_f32_e32 v58, s17, v50
	v_fmac_f32_e32 v59, s17, v51
	v_fmac_f32_e32 v60, s17, v52
	v_fmac_f32_e32 v61, s17, v53
	v_fmac_f32_e32 v62, s17, v54
	v_fmac_f32_e32 v63, s17, v55
	global_store_dwordx4 v3, v[56:59], s[10:11]
	global_store_dwordx4 v3, v[60:63], s[10:11] offset:16
	s_endpgm
	.p2align	8

	.amdhsa_kernel _Z9k_combinePKDF16_PK15HIP_vector_typeIiLj2EEPKS1_IfLj2EEPf
		.amdhsa_group_segment_fixed_size 0
		.amdhsa_private_segment_fixed_size 0
		.amdhsa_kernarg_size 32
		.amdhsa_user_sgpr_count 2
		.amdhsa_user_sgpr_dispatch_ptr 0
		.amdhsa_user_sgpr_queue_ptr 0
		.amdhsa_user_sgpr_kernarg_segment_ptr 1
		.amdhsa_user_sgpr_dispatch_id 0
		.amdhsa_user_sgpr_kernarg_preload_length 0
		.amdhsa_user_sgpr_kernarg_preload_offset 0
		.amdhsa_user_sgpr_private_segment_size 0
		.amdhsa_uses_dynamic_stack 0
		.amdhsa_enable_private_segment 0
		.amdhsa_system_sgpr_workgroup_id_x 1
		.amdhsa_system_sgpr_workgroup_id_y 0
		.amdhsa_system_sgpr_workgroup_id_z 0
		.amdhsa_system_sgpr_workgroup_info 0
		.amdhsa_system_vgpr_workitem_id 0
		.amdhsa_next_free_vgpr 64
		.amdhsa_next_free_sgpr 24
		.amdhsa_accum_offset 64
		.amdhsa_reserve_vcc 1
		.amdhsa_float_round_mode_32 0
		.amdhsa_float_round_mode_16_64 0
		.amdhsa_float_denorm_mode_32 3
		.amdhsa_float_denorm_mode_16_64 3
		.amdhsa_dx10_clamp 1
		.amdhsa_ieee_mode 1
		.amdhsa_fp16_overflow 0
		.amdhsa_tg_split 0
		.amdhsa_exception_fp_ieee_invalid_op 0
		.amdhsa_exception_fp_denorm_src 0
		.amdhsa_exception_fp_ieee_div_zero 0
		.amdhsa_exception_fp_ieee_overflow 0
		.amdhsa_exception_fp_ieee_underflow 0
		.amdhsa_exception_fp_ieee_inexact 0
		.amdhsa_exception_int_div_zero 0
	.end_amdhsa_kernel

.Lfunc_end3:
	.size	_Z9k_combinePKDF16_PK15HIP_vector_typeIiLj2EEPKS1_IfLj2EEPf, .Lfunc_end3-_Z9k_combinePKDF16_PK15HIP_vector_typeIiLj2EEPKS1_IfLj2EEPf
	.set _Z9k_combinePKDF16_PK15HIP_vector_typeIiLj2EEPKS1_IfLj2EEPf.num_vgpr, 64
	.set _Z9k_combinePKDF16_PK15HIP_vector_typeIiLj2EEPKS1_IfLj2EEPf.num_agpr, 0
	.set _Z9k_combinePKDF16_PK15HIP_vector_typeIiLj2EEPKS1_IfLj2EEPf.numbered_sgpr, 24
	.set _Z9k_combinePKDF16_PK15HIP_vector_typeIiLj2EEPKS1_IfLj2EEPf.num_named_barrier, 0
	.set _Z9k_combinePKDF16_PK15HIP_vector_typeIiLj2EEPKS1_IfLj2EEPf.private_seg_size, 0
	.set _Z9k_combinePKDF16_PK15HIP_vector_typeIiLj2EEPKS1_IfLj2EEPf.uses_vcc, 1
	.set _Z9k_combinePKDF16_PK15HIP_vector_typeIiLj2EEPKS1_IfLj2EEPf.uses_flat_scratch, 0
	.set _Z9k_combinePKDF16_PK15HIP_vector_typeIiLj2EEPKS1_IfLj2EEPf.has_dyn_sized_stack, 0
	.set _Z9k_combinePKDF16_PK15HIP_vector_typeIiLj2EEPKS1_IfLj2EEPf.has_recursion, 0
	.set _Z9k_combinePKDF16_PK15HIP_vector_typeIiLj2EEPKS1_IfLj2EEPf.has_indirect_call, 0

amdhsa.kernels:
  - .agpr_count:     0
    .args:
      - .actual_access:  read_only
        .address_space:  global
        .offset:         0
        .size:           8
        .value_kind:     global_buffer
      - .actual_access:  read_only
        .address_space:  global
        .offset:         8
        .size:           8
        .value_kind:     global_buffer
      - .actual_access:  write_only
        .address_space:  global
        .offset:         16
        .size:           8
        .value_kind:     global_buffer
      - .actual_access:  write_only
        .address_space:  global
        .offset:         24
        .size:           8
        .value_kind:     global_buffer
      - .actual_access:  write_only
        .address_space:  global
        .offset:         32
        .size:           8
        .value_kind:     global_buffer
      - .actual_access:  write_only
        .address_space:  global
        .offset:         40
        .size:           8
        .value_kind:     global_buffer
    .group_segment_fixed_size: 256
    .kernarg_segment_align: 8
    .kernarg_segment_size: 48
    .language:       OpenCL C
    .language_version:
      - 2
      - 0
    .max_flat_workgroup_size: 256
    .name:           _Z10k_xscatterPKiS0_P15HIP_vector_typeIiLj2EEPtP4MetaS3_
    .private_segment_fixed_size: 0
    .sgpr_count:     41
    .sgpr_spill_count: 0
    .symbol:         _Z10k_xscatterPKiS0_P15HIP_vector_typeIiLj2EEPtP4MetaS3_.kd
    .uniform_work_group_size: 1
    .uses_dynamic_stack: false
    .vgpr_count:     55
    .vgpr_spill_count: 0
    .wavefront_size: 64
  - .agpr_count:     0
    .args:
      - .actual_access:  read_only
        .address_space:  global
        .offset:         0
        .size:           8
        .value_kind:     global_buffer
      - .actual_access:  read_only
        .address_space:  global
        .offset:         8
        .size:           8
        .value_kind:     global_buffer
      - .actual_access:  write_only
        .address_space:  global
        .offset:         16
        .size:           8
        .value_kind:     global_buffer
      - .actual_access:  write_only
        .address_space:  global
        .offset:         24
        .size:           8
        .value_kind:     global_buffer
      - .actual_access:  write_only
        .address_space:  global
        .offset:         32
        .size:           8
        .value_kind:     global_buffer
      - .actual_access:  read_only
        .address_space:  global
        .offset:         40
        .size:           8
        .value_kind:     global_buffer
      - .actual_access:  read_only
        .address_space:  global
        .offset:         48
        .size:           8
        .value_kind:     global_buffer
      - .actual_access:  write_only
        .address_space:  global
        .offset:         56
        .size:           8
        .value_kind:     global_buffer
      - .actual_access:  write_only
        .address_space:  global
        .offset:         64
        .size:           8
        .value_kind:     global_buffer
    .group_segment_fixed_size: 4096
    .kernarg_segment_align: 8
    .kernarg_segment_size: 72
    .language:       OpenCL C
    .language_version:
      - 2
      - 0
    .max_flat_workgroup_size: 256
    .name:           _Z5k_prePKfS0_PiP15HIP_vector_typeIfLj2EES1_S0_S0_PDF16_S5_
    .private_segment_fixed_size: 0
    .sgpr_count:     38
    .sgpr_spill_count: 0
    .symbol:         _Z5k_prePKfS0_PiP15HIP_vector_typeIfLj2EES1_S0_S0_PDF16_S5_.kd
    .uniform_work_group_size: 1
    .uses_dynamic_stack: false
    .vgpr_count:     128
    .vgpr_spill_count: 0
    .wavefront_size: 64
  - .agpr_count:     0
    .args:
      - .address_space:  global
        .offset:         0
        .size:           8
        .value_kind:     global_buffer
      - .address_space:  global
        .offset:         8
        .size:           8
        .value_kind:     global_buffer
      - .actual_access:  write_only
        .address_space:  global
        .offset:         16
        .size:           8
        .value_kind:     global_buffer
      - .actual_access:  read_only
        .address_space:  global
        .offset:         24
        .size:           8
        .value_kind:     global_buffer
    .group_segment_fixed_size: 0
    .kernarg_segment_align: 8
    .kernarg_segment_size: 32
    .language:       OpenCL C
    .language_version:
      - 2
      - 0
    .max_flat_workgroup_size: 512
    .name:           _Z7k_gemm2PKDF16_S0_PDF16_PK15HIP_vector_typeIiLj2EE
    .private_segment_fixed_size: 0
    .sgpr_count:     74
    .sgpr_spill_count: 0
    .symbol:         _Z7k_gemm2PKDF16_S0_PDF16_PK15HIP_vector_typeIiLj2EE.kd
    .uniform_work_group_size: 1
    .uses_dynamic_stack: false
    .vgpr_count:     226
    .vgpr_spill_count: 0
    .wavefront_size: 64
  - .agpr_count:     0
    .args:
      - .actual_access:  read_only
        .address_space:  global
        .offset:         0
        .size:           8
        .value_kind:     global_buffer
      - .actual_access:  read_only
        .address_space:  global
        .offset:         8
        .size:           8
        .value_kind:     global_buffer
      - .actual_access:  read_only
        .address_space:  global
        .offset:         16
        .size:           8
        .value_kind:     global_buffer
      - .actual_access:  write_only
        .address_space:  global
        .offset:         24
        .size:           8
        .value_kind:     global_buffer
    .group_segment_fixed_size: 0
    .kernarg_segment_align: 8
    .kernarg_segment_size: 32
    .language:       OpenCL C
    .language_version:
      - 2
      - 0
    .max_flat_workgroup_size: 256
    .name:           _Z9k_combinePKDF16_PK15HIP_vector_typeIiLj2EEPKS1_IfLj2EEPf
    .private_segment_fixed_size: 0
    .sgpr_count:     30
    .sgpr_spill_count: 0
    .symbol:         _Z9k_combinePKDF16_PK15HIP_vector_typeIiLj2EEPKS1_IfLj2EEPf.kd
    .uniform_work_group_size: 1
    .uses_dynamic_stack: false
    .vgpr_count:     64
    .vgpr_spill_count: 0
    .wavefront_size: 64
  - .agpr_count:     0
    .args:
      - .address_space:  global
        .offset:         0
        .size:           8
        .value_kind:     global_buffer
      - .address_space:  global
        .offset:         8
        .size:           8
        .value_kind:     global_buffer
      - .actual_access:  write_only
        .address_space:  global
        .offset:         16
        .size:           8
        .value_kind:     global_buffer
      - .actual_access:  read_only
        .address_space:  global
        .offset:         24
        .size:           8
        .value_kind:     global_buffer
      - .address_space:  global
        .offset:         32
        .size:           8
        .value_kind:     global_buffer
      - .address_space:  global
        .offset:         40
        .size:           8
        .value_kind:     global_buffer
      - .actual_access:  write_only
        .address_space:  global
        .offset:         48
        .size:           8
        .value_kind:     global_buffer
      - .address_space:  global
        .offset:         56
        .size:           8
        .value_kind:     global_buffer
    .group_segment_fixed_size: 0
    .kernarg_segment_align: 8
    .kernarg_segment_size: 64
    .language:       OpenCL C
    .language_version:
      - 2
      - 0
    .max_flat_workgroup_size: 512
    .name:           _Z7k_gemm1ILi0EEvPKDF16_S1_PDF16_PK15HIP_vector_typeIiLj2EEPKfS8_S2_PKt
    .private_segment_fixed_size: 0
    .sgpr_count:     100
    .sgpr_spill_count: 0
    .symbol:         _Z7k_gemm1ILi0EEvPKDF16_S1_PDF16_PK15HIP_vector_typeIiLj2EEPKfS8_S2_PKt.kd
    .uniform_work_group_size: 1
    .uses_dynamic_stack: false
    .vgpr_count:     256
    .vgpr_spill_count: 0
    .wavefront_size: 64
  - .agpr_count:     0
    .args:
      - .address_space:  global
        .offset:         0
        .size:           8
        .value_kind:     global_buffer
      - .address_space:  global
        .offset:         8
        .size:           8
        .value_kind:     global_buffer
      - .actual_access:  write_only
        .address_space:  global
        .offset:         16
        .size:           8
        .value_kind:     global_buffer
      - .actual_access:  read_only
        .address_space:  global
        .offset:         24
        .size:           8
        .value_kind:     global_buffer
      - .address_space:  global
        .offset:         32
        .size:           8
        .value_kind:     global_buffer
      - .actual_access:  read_only
        .address_space:  global
        .offset:         40
        .size:           8
        .value_kind:     global_buffer
      - .actual_access:  write_only
        .address_space:  global
        .offset:         48
        .size:           8
        .value_kind:     global_buffer
      - .address_space:  global
        .offset:         56
        .size:           8
        .value_kind:     global_buffer
    .group_segment_fixed_size: 0
    .kernarg_segment_align: 8
    .kernarg_segment_size: 64
    .language:       OpenCL C
    .language_version:
      - 2
      - 0
    .max_flat_workgroup_size: 512
    .name:           _Z7k_gemm1ILi1EEvPKDF16_S1_PDF16_PK15HIP_vector_typeIiLj2EEPKfS8_S2_PKt
    .private_segment_fixed_size: 0
    .sgpr_count:     94
    .sgpr_spill_count: 0
    .symbol:         _Z7k_gemm1ILi1EEvPKDF16_S1_PDF16_PK15HIP_vector_typeIiLj2EEPKfS8_S2_PKt.kd
    .uniform_work_group_size: 1
    .uses_dynamic_stack: false
    .vgpr_count:     254
    .vgpr_spill_count: 0
    .wavefront_size: 64
